# t25
# speedup vs baseline: 1.0257x; 1.0224x over previous
_Z11align_fusedPKfS0_PKiPf:
	s_load_dwordx8 s[4:11], s[0:1], 0x0
	s_sub_u32 s2, 0x1fff, s2
	s_mul_i32 s12, s2, 0x5dc0
	v_and_b32_e32 v7, 63, v0
	v_readfirstlane_b32 s13, v0
	v_lshlrev_b32_e32 v1, 4, v7
	v_mul_u32_u24_e32 v3, 12, v7
	s_mul_i32 s18, s13, 96
	s_mul_i32 s3, s13, 6
	s_sub_u32 s3, 0x49c, s3
	v_cmp_gt_u32_e64 s[14:15], s3, v7
	v_add_u32_e32 v2, s18, v1
	v_add_u32_e32 v3, s18, v3
	v_add_u32_e32 v4, 0x600, v3
	s_add_u32 s12, s12, s18
	s_add_u32 s12, s12, 0x800
	s_waitcnt lgkmcnt(0)
	s_sub_u32 s44, s12, 0x800
	s_add_u32 s40, s4, s44
	s_addc_u32 s41, s5, 0
	s_add_u32 s42, s40, 0x1000
	s_addc_u32 s43, s41, 0
	s_add_u32 s4, s4, s12
	s_addc_u32 s5, s5, 0
	s_add_u32 s10, s10, s12
	s_addc_u32 s11, s11, 0
	s_cmp_lg_u32 s13, 0
	s_cbranch_scc1 .Lbulk_waves
	v_lshlrev_b32_e32 v5, 2, v7
	global_load_dword v5, v5, s[8:9]
	global_load_dwordx3 v[44:46], v3, s[6:7]
	s_mov_b32 m0, s18
	s_nop 0
	global_load_lds_dwordx4 v1, s[40:41] sc1 nt
	global_load_lds_dwordx4 v1, s[40:41] offset:1024 sc1 nt
	global_load_lds_dwordx4 v1, s[40:41] offset:2048 sc1 nt
	global_load_lds_dwordx4 v1, s[40:41] offset:3072 sc1 nt
	s_add_u32 m0, s18, 0x1000
	s_nop 0
	global_load_lds_dwordx4 v1, s[42:43] sc1 nt
	global_load_lds_dwordx4 v1, s[42:43] offset:1024 sc1 nt
	s_mov_b32 s20, 0
	s_mov_b32 s21, 0x10000
	s_mov_b32 s22, 0
	s_mov_b32 s23, 0x20000
	s_mov_b32 s24, 0
	s_mov_b32 s25, 0x40000
	s_mov_b32 s26, 0
	s_mov_b32 s27, 0x80000
	s_waitcnt vmcnt(6)
	v_mul_u32_u24_e32 v5, 12, v5
	v_add_f32_dpp v52, v44, v44 quad_perm:[1,0,3,2] row_mask:0xf bank_mask:0xf
	v_add_f32_dpp v53, v45, v45 quad_perm:[1,0,3,2] row_mask:0xf bank_mask:0xf
	v_add_f32_dpp v54, v46, v46 quad_perm:[1,0,3,2] row_mask:0xf bank_mask:0xf
	v_add_f32_dpp v52, v52, v52 quad_perm:[2,3,0,1] row_mask:0xf bank_mask:0xf
	v_add_f32_dpp v53, v53, v53 quad_perm:[2,3,0,1] row_mask:0xf bank_mask:0xf
	v_add_f32_dpp v54, v54, v54 quad_perm:[2,3,0,1] row_mask:0xf bank_mask:0xf
	v_add_f32_dpp v52, v52, v52 row_half_mirror row_mask:0xf bank_mask:0xf
	v_add_f32_dpp v53, v53, v53 row_half_mirror row_mask:0xf bank_mask:0xf
	v_add_f32_dpp v54, v54, v54 row_half_mirror row_mask:0xf bank_mask:0xf
	v_add_f32_dpp v52, v52, v52 row_mirror row_mask:0xf bank_mask:0xf
	v_add_f32_dpp v53, v53, v53 row_mirror row_mask:0xf bank_mask:0xf
	v_add_f32_dpp v54, v54, v54 row_mirror row_mask:0xf bank_mask:0xf
	v_add_f32_dpp v52, v52, v52 row_bcast:15 row_mask:0xa bank_mask:0xf
	v_add_f32_dpp v53, v53, v53 row_bcast:15 row_mask:0xa bank_mask:0xf
	v_add_f32_dpp v54, v54, v54 row_bcast:15 row_mask:0xa bank_mask:0xf
	v_add_f32_dpp v52, v52, v52 row_bcast:31 row_mask:0xc bank_mask:0xf
	v_add_f32_dpp v53, v53, v53 row_bcast:31 row_mask:0xc bank_mask:0xf
	v_add_f32_dpp v54, v54, v54 row_bcast:31 row_mask:0xc bank_mask:0xf
	v_readlane_b32 s28, v52, 63
	v_readlane_b32 s29, v53, 63
	v_readlane_b32 s30, v54, 63
	v_mov_b32_e32 v52, s28
	v_mov_b32_e32 v53, s29
	v_mov_b32_e32 v54, s30
	v_fmac_f32_e32 v44, 0xbc800000, v52
	v_fmac_f32_e32 v45, 0xbc800000, v53
	v_fmac_f32_e32 v46, 0xbc800000, v54
	s_waitcnt vmcnt(0)
	s_waitcnt lgkmcnt(0)
	s_barrier
	ds_read_b32 v48, v5
	ds_read_b32 v49, v5 offset:4
	ds_read_b32 v50, v5 offset:8
	s_waitcnt lgkmcnt(0)
	v_add_f32_dpp v52, v48, v48 quad_perm:[1,0,3,2] row_mask:0xf bank_mask:0xf
	v_add_f32_dpp v53, v49, v49 quad_perm:[1,0,3,2] row_mask:0xf bank_mask:0xf
	v_add_f32_dpp v54, v50, v50 quad_perm:[1,0,3,2] row_mask:0xf bank_mask:0xf
	v_add_f32_dpp v52, v52, v52 quad_perm:[2,3,0,1] row_mask:0xf bank_mask:0xf
	v_add_f32_dpp v53, v53, v53 quad_perm:[2,3,0,1] row_mask:0xf bank_mask:0xf
	v_add_f32_dpp v54, v54, v54 quad_perm:[2,3,0,1] row_mask:0xf bank_mask:0xf
	v_add_f32_dpp v52, v52, v52 row_half_mirror row_mask:0xf bank_mask:0xf
	v_add_f32_dpp v53, v53, v53 row_half_mirror row_mask:0xf bank_mask:0xf
	v_add_f32_dpp v54, v54, v54 row_half_mirror row_mask:0xf bank_mask:0xf
	v_add_f32_dpp v52, v52, v52 row_mirror row_mask:0xf bank_mask:0xf
	v_add_f32_dpp v53, v53, v53 row_mirror row_mask:0xf bank_mask:0xf
	v_add_f32_dpp v54, v54, v54 row_mirror row_mask:0xf bank_mask:0xf
	v_add_f32_dpp v52, v52, v52 row_bcast:15 row_mask:0xa bank_mask:0xf
	v_add_f32_dpp v53, v53, v53 row_bcast:15 row_mask:0xa bank_mask:0xf
	v_add_f32_dpp v54, v54, v54 row_bcast:15 row_mask:0xa bank_mask:0xf
	v_add_f32_dpp v52, v52, v52 row_bcast:31 row_mask:0xc bank_mask:0xf
	v_add_f32_dpp v53, v53, v53 row_bcast:31 row_mask:0xc bank_mask:0xf
	v_add_f32_dpp v54, v54, v54 row_bcast:31 row_mask:0xc bank_mask:0xf
	v_readlane_b32 s32, v52, 63
	v_readlane_b32 s33, v53, 63
	v_readlane_b32 s34, v54, 63
	v_mov_b32_e32 v52, s32
	v_mov_b32_e32 v53, s33
	v_mov_b32_e32 v54, s34
	v_fmac_f32_e32 v48, 0xbc800000, v52
	v_fmac_f32_e32 v49, 0xbc800000, v53
	v_fmac_f32_e32 v50, 0xbc800000, v54
	v_mul_f32_e32 v52, v48, v44
	v_mul_f32_e32 v53, v48, v45
	v_mul_f32_e32 v54, v48, v46
	v_mul_f32_e32 v55, v49, v44
	v_mul_f32_e32 v56, v49, v45
	v_mul_f32_e32 v57, v49, v46
	v_mul_f32_e32 v58, v50, v44
	v_mul_f32_e32 v59, v50, v45
	v_mul_f32_e32 v60, v50, v46
	v_add_f32_dpp v52, v52, v52 quad_perm:[1,0,3,2] row_mask:0xf bank_mask:0xf
	v_add_f32_dpp v53, v53, v53 quad_perm:[1,0,3,2] row_mask:0xf bank_mask:0xf
	v_add_f32_dpp v54, v54, v54 quad_perm:[1,0,3,2] row_mask:0xf bank_mask:0xf
	v_add_f32_dpp v55, v55, v55 quad_perm:[1,0,3,2] row_mask:0xf bank_mask:0xf
	v_add_f32_dpp v56, v56, v56 quad_perm:[1,0,3,2] row_mask:0xf bank_mask:0xf
	v_add_f32_dpp v57, v57, v57 quad_perm:[1,0,3,2] row_mask:0xf bank_mask:0xf
	v_add_f32_dpp v58, v58, v58 quad_perm:[1,0,3,2] row_mask:0xf bank_mask:0xf
	v_add_f32_dpp v59, v59, v59 quad_perm:[1,0,3,2] row_mask:0xf bank_mask:0xf
	v_add_f32_dpp v60, v60, v60 quad_perm:[1,0,3,2] row_mask:0xf bank_mask:0xf
	v_add_f32_dpp v52, v52, v52 quad_perm:[2,3,0,1] row_mask:0xf bank_mask:0xf
	v_add_f32_dpp v53, v53, v53 quad_perm:[2,3,0,1] row_mask:0xf bank_mask:0xf
	v_add_f32_dpp v54, v54, v54 quad_perm:[2,3,0,1] row_mask:0xf bank_mask:0xf
	v_add_f32_dpp v55, v55, v55 quad_perm:[2,3,0,1] row_mask:0xf bank_mask:0xf
	v_add_f32_dpp v56, v56, v56 quad_perm:[2,3,0,1] row_mask:0xf bank_mask:0xf
	v_add_f32_dpp v57, v57, v57 quad_perm:[2,3,0,1] row_mask:0xf bank_mask:0xf
	v_add_f32_dpp v58, v58, v58 quad_perm:[2,3,0,1] row_mask:0xf bank_mask:0xf
	v_add_f32_dpp v59, v59, v59 quad_perm:[2,3,0,1] row_mask:0xf bank_mask:0xf
	v_add_f32_dpp v60, v60, v60 quad_perm:[2,3,0,1] row_mask:0xf bank_mask:0xf
	v_add_f32_dpp v52, v52, v52 row_half_mirror row_mask:0xf bank_mask:0xf
	v_add_f32_dpp v53, v53, v53 row_half_mirror row_mask:0xf bank_mask:0xf
	v_add_f32_dpp v54, v54, v54 row_half_mirror row_mask:0xf bank_mask:0xf
	v_add_f32_dpp v55, v55, v55 row_half_mirror row_mask:0xf bank_mask:0xf
	v_add_f32_dpp v56, v56, v56 row_half_mirror row_mask:0xf bank_mask:0xf
	v_add_f32_dpp v57, v57, v57 row_half_mirror row_mask:0xf bank_mask:0xf
	v_add_f32_dpp v58, v58, v58 row_half_mirror row_mask:0xf bank_mask:0xf
	v_add_f32_dpp v59, v59, v59 row_half_mirror row_mask:0xf bank_mask:0xf
	v_add_f32_dpp v60, v60, v60 row_half_mirror row_mask:0xf bank_mask:0xf
	v_add_f32_dpp v52, v52, v52 row_mirror row_mask:0xf bank_mask:0xf
	v_add_f32_dpp v53, v53, v53 row_mirror row_mask:0xf bank_mask:0xf
	v_add_f32_dpp v54, v54, v54 row_mirror row_mask:0xf bank_mask:0xf
	v_add_f32_dpp v55, v55, v55 row_mirror row_mask:0xf bank_mask:0xf
	v_add_f32_dpp v56, v56, v56 row_mirror row_mask:0xf bank_mask:0xf
	v_add_f32_dpp v57, v57, v57 row_mirror row_mask:0xf bank_mask:0xf
	v_add_f32_dpp v58, v58, v58 row_mirror row_mask:0xf bank_mask:0xf
	v_add_f32_dpp v59, v59, v59 row_mirror row_mask:0xf bank_mask:0xf
	v_add_f32_dpp v60, v60, v60 row_mirror row_mask:0xf bank_mask:0xf
	v_add_f32_dpp v52, v52, v52 row_bcast:15 row_mask:0xa bank_mask:0xf
	v_add_f32_dpp v53, v53, v53 row_bcast:15 row_mask:0xa bank_mask:0xf
	v_add_f32_dpp v54, v54, v54 row_bcast:15 row_mask:0xa bank_mask:0xf
	v_add_f32_dpp v55, v55, v55 row_bcast:15 row_mask:0xa bank_mask:0xf
	v_add_f32_dpp v56, v56, v56 row_bcast:15 row_mask:0xa bank_mask:0xf
	v_add_f32_dpp v57, v57, v57 row_bcast:15 row_mask:0xa bank_mask:0xf
	v_add_f32_dpp v58, v58, v58 row_bcast:15 row_mask:0xa bank_mask:0xf
	v_add_f32_dpp v59, v59, v59 row_bcast:15 row_mask:0xa bank_mask:0xf
	v_add_f32_dpp v60, v60, v60 row_bcast:15 row_mask:0xa bank_mask:0xf
	v_add_f32_dpp v52, v52, v52 row_bcast:31 row_mask:0xc bank_mask:0xf
	v_add_f32_dpp v53, v53, v53 row_bcast:31 row_mask:0xc bank_mask:0xf
	v_add_f32_dpp v54, v54, v54 row_bcast:31 row_mask:0xc bank_mask:0xf
	v_add_f32_dpp v55, v55, v55 row_bcast:31 row_mask:0xc bank_mask:0xf
	v_add_f32_dpp v56, v56, v56 row_bcast:31 row_mask:0xc bank_mask:0xf
	v_add_f32_dpp v57, v57, v57 row_bcast:31 row_mask:0xc bank_mask:0xf
	v_add_f32_dpp v58, v58, v58 row_bcast:31 row_mask:0xc bank_mask:0xf
	v_add_f32_dpp v59, v59, v59 row_bcast:31 row_mask:0xc bank_mask:0xf
	v_add_f32_dpp v60, v60, v60 row_bcast:31 row_mask:0xc bank_mask:0xf
	v_cndmask_b32_e64 v52, v52, v55, s[22:23]
	v_cndmask_b32_e64 v53, v53, v56, s[22:23]
	v_cndmask_b32_e64 v54, v54, v57, s[22:23]
	v_cndmask_b32_e64 v52, v52, v58, s[24:25]
	v_cndmask_b32_e64 v53, v53, v59, s[24:25]
	v_cndmask_b32_e64 v54, v54, v60, s[24:25]
	v_cndmask_b32_e64 v52, v52, 0, s[26:27]
	v_cndmask_b32_e64 v53, v53, 0, s[26:27]
	v_cndmask_b32_e64 v54, v54, 0, s[26:27]
	v_cndmask_b32_e64 v40, 0, 1.0, s[20:21]
	v_cndmask_b32_e64 v41, 0, 1.0, s[22:23]
	v_cndmask_b32_e64 v42, 0, 1.0, s[24:25]
	v_mul_f32_e32 v55, v52, v52
	v_mul_f32_e32 v56, v53, v53
	v_mul_f32_e32 v57, v52, v53
	v_add_f32_dpp v55, v55, v55 quad_perm:[1,0,3,2] row_mask:0xf bank_mask:0xf
	v_add_f32_dpp v56, v56, v56 quad_perm:[1,0,3,2] row_mask:0xf bank_mask:0xf
	v_add_f32_dpp v57, v57, v57 quad_perm:[1,0,3,2] row_mask:0xf bank_mask:0xf
	v_add_f32_dpp v55, v55, v55 quad_perm:[2,3,0,1] row_mask:0xf bank_mask:0xf
	v_add_f32_dpp v56, v56, v56 quad_perm:[2,3,0,1] row_mask:0xf bank_mask:0xf
	v_add_f32_dpp v57, v57, v57 quad_perm:[2,3,0,1] row_mask:0xf bank_mask:0xf
	v_sub_f32_e32 v60, v56, v55
	v_mul_f32_e32 v58, v57, v57
	v_cmp_gt_f32_e32 vcc, 0, v60
	v_mul_f32_e32 v59, v60, v60
	v_fmac_f32_e32 v59, 4.0, v58
	v_sqrt_f32_e32 v59, v59
	s_nop 0
	v_add_f32_e64 v59, |v60|, v59
	v_add_f32_e32 v59, 0x0da24260, v59
	v_rcp_f32_e32 v59, v59
	v_add_f32_e32 v58, v57, v57
	v_mul_f32_e32 v59, v58, v59
	v_cndmask_b32_e64 v59, v59, -v59, vcc
	v_fma_f32 v58, v59, v59, 1.0
	v_rsq_f32_e32 v61, v58
	s_nop 0
	v_mul_f32_e32 v62, v61, v59
	v_mul_f32_e32 v55, v62, v53
	v_mul_f32_e32 v56, v62, v52
	v_fma_f32 v52, v61, v52, -v55
	v_fma_f32 v53, v61, v53, v56
	v_mul_f32_e32 v55, v52, v52
	v_mul_f32_e32 v56, v54, v54
	v_mul_f32_e32 v57, v52, v54
	v_add_f32_dpp v55, v55, v55 quad_perm:[1,0,3,2] row_mask:0xf bank_mask:0xf
	v_add_f32_dpp v56, v56, v56 quad_perm:[1,0,3,2] row_mask:0xf bank_mask:0xf
	v_add_f32_dpp v57, v57, v57 quad_perm:[1,0,3,2] row_mask:0xf bank_mask:0xf
	v_add_f32_dpp v55, v55, v55 quad_perm:[2,3,0,1] row_mask:0xf bank_mask:0xf
	v_add_f32_dpp v56, v56, v56 quad_perm:[2,3,0,1] row_mask:0xf bank_mask:0xf
	v_add_f32_dpp v57, v57, v57 quad_perm:[2,3,0,1] row_mask:0xf bank_mask:0xf
	v_sub_f32_e32 v60, v56, v55
	v_mul_f32_e32 v58, v57, v57
	v_cmp_gt_f32_e32 vcc, 0, v60
	v_mul_f32_e32 v59, v60, v60
	v_fmac_f32_e32 v59, 4.0, v58
	v_sqrt_f32_e32 v59, v59
	v_mul_f32_e32 v63, v62, v41
	v_mul_f32_e32 v43, v62, v40
	v_fma_f32 v40, v61, v40, -v63
	v_fma_f32 v41, v61, v41, v43
	v_add_f32_e64 v59, |v60|, v59
	v_add_f32_e32 v59, 0x0da24260, v59
	v_rcp_f32_e32 v59, v59
	v_add_f32_e32 v58, v57, v57
	v_mul_f32_e32 v59, v58, v59
	v_cndmask_b32_e64 v59, v59, -v59, vcc
	v_fma_f32 v58, v59, v59, 1.0
	v_rsq_f32_e32 v61, v58
	s_nop 0
	v_mul_f32_e32 v62, v61, v59
	v_mul_f32_e32 v55, v62, v54
	v_mul_f32_e32 v56, v62, v52
	v_fma_f32 v52, v61, v52, -v55
	v_fma_f32 v54, v61, v54, v56
	v_mul_f32_e32 v55, v53, v53
	v_mul_f32_e32 v56, v54, v54
	v_mul_f32_e32 v57, v53, v54
	v_add_f32_dpp v55, v55, v55 quad_perm:[1,0,3,2] row_mask:0xf bank_mask:0xf
	v_add_f32_dpp v56, v56, v56 quad_perm:[1,0,3,2] row_mask:0xf bank_mask:0xf
	v_add_f32_dpp v57, v57, v57 quad_perm:[1,0,3,2] row_mask:0xf bank_mask:0xf
	v_add_f32_dpp v55, v55, v55 quad_perm:[2,3,0,1] row_mask:0xf bank_mask:0xf
	v_add_f32_dpp v56, v56, v56 quad_perm:[2,3,0,1] row_mask:0xf bank_mask:0xf
	v_add_f32_dpp v57, v57, v57 quad_perm:[2,3,0,1] row_mask:0xf bank_mask:0xf
	v_sub_f32_e32 v60, v56, v55
	v_mul_f32_e32 v58, v57, v57
	v_cmp_gt_f32_e32 vcc, 0, v60
	v_mul_f32_e32 v59, v60, v60
	v_fmac_f32_e32 v59, 4.0, v58
	v_sqrt_f32_e32 v59, v59
	v_mul_f32_e32 v63, v62, v42
	v_mul_f32_e32 v43, v62, v40
	v_fma_f32 v40, v61, v40, -v63
	v_fma_f32 v42, v61, v42, v43
	v_add_f32_e64 v59, |v60|, v59
	v_add_f32_e32 v59, 0x0da24260, v59
	v_rcp_f32_e32 v59, v59
	v_add_f32_e32 v58, v57, v57
	v_mul_f32_e32 v59, v58, v59
	v_cndmask_b32_e64 v59, v59, -v59, vcc
	v_fma_f32 v58, v59, v59, 1.0
	v_rsq_f32_e32 v61, v58
	s_nop 0
	v_mul_f32_e32 v62, v61, v59
	v_mul_f32_e32 v55, v62, v54
	v_mul_f32_e32 v56, v62, v53
	v_fma_f32 v53, v61, v53, -v55
	v_fma_f32 v54, v61, v54, v56
	v_mul_f32_e32 v55, v52, v52
	v_mul_f32_e32 v56, v53, v53
	v_mul_f32_e32 v57, v52, v53
	v_add_f32_dpp v55, v55, v55 quad_perm:[1,0,3,2] row_mask:0xf bank_mask:0xf
	v_add_f32_dpp v56, v56, v56 quad_perm:[1,0,3,2] row_mask:0xf bank_mask:0xf
	v_add_f32_dpp v57, v57, v57 quad_perm:[1,0,3,2] row_mask:0xf bank_mask:0xf
	v_add_f32_dpp v55, v55, v55 quad_perm:[2,3,0,1] row_mask:0xf bank_mask:0xf
	v_add_f32_dpp v56, v56, v56 quad_perm:[2,3,0,1] row_mask:0xf bank_mask:0xf
	v_add_f32_dpp v57, v57, v57 quad_perm:[2,3,0,1] row_mask:0xf bank_mask:0xf
	v_sub_f32_e32 v60, v56, v55
	v_mul_f32_e32 v58, v57, v57
	v_cmp_gt_f32_e32 vcc, 0, v60
	v_mul_f32_e32 v59, v60, v60
	v_fmac_f32_e32 v59, 4.0, v58
	v_sqrt_f32_e32 v59, v59
	v_mul_f32_e32 v63, v62, v42
	v_mul_f32_e32 v43, v62, v41
	v_fma_f32 v41, v61, v41, -v63
	v_fma_f32 v42, v61, v42, v43
	v_add_f32_e64 v59, |v60|, v59
	v_add_f32_e32 v59, 0x0da24260, v59
	v_rcp_f32_e32 v59, v59
	v_add_f32_e32 v58, v57, v57
	v_mul_f32_e32 v59, v58, v59
	v_cndmask_b32_e64 v59, v59, -v59, vcc
	v_fma_f32 v58, v59, v59, 1.0
	v_rsq_f32_e32 v61, v58
	s_nop 0
	v_mul_f32_e32 v62, v61, v59
	v_mul_f32_e32 v55, v62, v53
	v_mul_f32_e32 v56, v62, v52
	v_fma_f32 v52, v61, v52, -v55
	v_fma_f32 v53, v61, v53, v56
	v_mul_f32_e32 v55, v52, v52
	v_mul_f32_e32 v56, v54, v54
	v_mul_f32_e32 v57, v52, v54
	v_add_f32_dpp v55, v55, v55 quad_perm:[1,0,3,2] row_mask:0xf bank_mask:0xf
	v_add_f32_dpp v56, v56, v56 quad_perm:[1,0,3,2] row_mask:0xf bank_mask:0xf
	v_add_f32_dpp v57, v57, v57 quad_perm:[1,0,3,2] row_mask:0xf bank_mask:0xf
	v_add_f32_dpp v55, v55, v55 quad_perm:[2,3,0,1] row_mask:0xf bank_mask:0xf
	v_add_f32_dpp v56, v56, v56 quad_perm:[2,3,0,1] row_mask:0xf bank_mask:0xf
	v_add_f32_dpp v57, v57, v57 quad_perm:[2,3,0,1] row_mask:0xf bank_mask:0xf
	v_sub_f32_e32 v60, v56, v55
	v_mul_f32_e32 v58, v57, v57
	v_cmp_gt_f32_e32 vcc, 0, v60
	v_mul_f32_e32 v59, v60, v60
	v_fmac_f32_e32 v59, 4.0, v58
	v_sqrt_f32_e32 v59, v59
	v_mul_f32_e32 v63, v62, v41
	v_mul_f32_e32 v43, v62, v40
	v_fma_f32 v40, v61, v40, -v63
	v_fma_f32 v41, v61, v41, v43
	v_add_f32_e64 v59, |v60|, v59
	v_add_f32_e32 v59, 0x0da24260, v59
	v_rcp_f32_e32 v59, v59
	v_add_f32_e32 v58, v57, v57
	v_mul_f32_e32 v59, v58, v59
	v_cndmask_b32_e64 v59, v59, -v59, vcc
	v_fma_f32 v58, v59, v59, 1.0
	v_rsq_f32_e32 v61, v58
	s_nop 0
	v_mul_f32_e32 v62, v61, v59
	v_mul_f32_e32 v55, v62, v54
	v_mul_f32_e32 v56, v62, v52
	v_fma_f32 v52, v61, v52, -v55
	v_fma_f32 v54, v61, v54, v56
	v_mul_f32_e32 v55, v53, v53
	v_mul_f32_e32 v56, v54, v54
	v_mul_f32_e32 v57, v53, v54
	v_add_f32_dpp v55, v55, v55 quad_perm:[1,0,3,2] row_mask:0xf bank_mask:0xf
	v_add_f32_dpp v56, v56, v56 quad_perm:[1,0,3,2] row_mask:0xf bank_mask:0xf
	v_add_f32_dpp v57, v57, v57 quad_perm:[1,0,3,2] row_mask:0xf bank_mask:0xf
	v_add_f32_dpp v55, v55, v55 quad_perm:[2,3,0,1] row_mask:0xf bank_mask:0xf
	v_add_f32_dpp v56, v56, v56 quad_perm:[2,3,0,1] row_mask:0xf bank_mask:0xf
	v_add_f32_dpp v57, v57, v57 quad_perm:[2,3,0,1] row_mask:0xf bank_mask:0xf
	v_sub_f32_e32 v60, v56, v55
	v_mul_f32_e32 v58, v57, v57
	v_cmp_gt_f32_e32 vcc, 0, v60
	v_mul_f32_e32 v59, v60, v60
	v_fmac_f32_e32 v59, 4.0, v58
	v_sqrt_f32_e32 v59, v59
	v_mul_f32_e32 v63, v62, v42
	v_mul_f32_e32 v43, v62, v40
	v_fma_f32 v40, v61, v40, -v63
	v_fma_f32 v42, v61, v42, v43
	v_add_f32_e64 v59, |v60|, v59
	v_add_f32_e32 v59, 0x0da24260, v59
	v_rcp_f32_e32 v59, v59
	v_add_f32_e32 v58, v57, v57
	v_mul_f32_e32 v59, v58, v59
	v_cndmask_b32_e64 v59, v59, -v59, vcc
	v_fma_f32 v58, v59, v59, 1.0
	v_rsq_f32_e32 v61, v58
	s_nop 0
	v_mul_f32_e32 v62, v61, v59
	v_mul_f32_e32 v55, v62, v54
	v_mul_f32_e32 v56, v62, v53
	v_fma_f32 v53, v61, v53, -v55
	v_fma_f32 v54, v61, v54, v56
	v_mul_f32_e32 v55, v52, v52
	v_mul_f32_e32 v56, v53, v53
	v_mul_f32_e32 v57, v52, v53
	v_add_f32_dpp v55, v55, v55 quad_perm:[1,0,3,2] row_mask:0xf bank_mask:0xf
	v_add_f32_dpp v56, v56, v56 quad_perm:[1,0,3,2] row_mask:0xf bank_mask:0xf
	v_add_f32_dpp v57, v57, v57 quad_perm:[1,0,3,2] row_mask:0xf bank_mask:0xf
	v_add_f32_dpp v55, v55, v55 quad_perm:[2,3,0,1] row_mask:0xf bank_mask:0xf
	v_add_f32_dpp v56, v56, v56 quad_perm:[2,3,0,1] row_mask:0xf bank_mask:0xf
	v_add_f32_dpp v57, v57, v57 quad_perm:[2,3,0,1] row_mask:0xf bank_mask:0xf
	v_sub_f32_e32 v60, v56, v55
	v_mul_f32_e32 v58, v57, v57
	v_cmp_gt_f32_e32 vcc, 0, v60
	v_mul_f32_e32 v59, v60, v60
	v_fmac_f32_e32 v59, 4.0, v58
	v_sqrt_f32_e32 v59, v59
	v_mul_f32_e32 v63, v62, v42
	v_mul_f32_e32 v43, v62, v41
	v_fma_f32 v41, v61, v41, -v63
	v_fma_f32 v42, v61, v42, v43
	v_add_f32_e64 v59, |v60|, v59
	v_add_f32_e32 v59, 0x0da24260, v59
	v_rcp_f32_e32 v59, v59
	v_add_f32_e32 v58, v57, v57
	v_mul_f32_e32 v59, v58, v59
	v_cndmask_b32_e64 v59, v59, -v59, vcc
	v_fma_f32 v58, v59, v59, 1.0
	v_rsq_f32_e32 v61, v58
	s_nop 0
	v_mul_f32_e32 v62, v61, v59
	v_mul_f32_e32 v55, v62, v53
	v_mul_f32_e32 v56, v62, v52
	v_fma_f32 v52, v61, v52, -v55
	v_fma_f32 v53, v61, v53, v56
	v_mul_f32_e32 v55, v52, v52
	v_mul_f32_e32 v56, v54, v54
	v_mul_f32_e32 v57, v52, v54
	v_add_f32_dpp v55, v55, v55 quad_perm:[1,0,3,2] row_mask:0xf bank_mask:0xf
	v_add_f32_dpp v56, v56, v56 quad_perm:[1,0,3,2] row_mask:0xf bank_mask:0xf
	v_add_f32_dpp v57, v57, v57 quad_perm:[1,0,3,2] row_mask:0xf bank_mask:0xf
	v_add_f32_dpp v55, v55, v55 quad_perm:[2,3,0,1] row_mask:0xf bank_mask:0xf
	v_add_f32_dpp v56, v56, v56 quad_perm:[2,3,0,1] row_mask:0xf bank_mask:0xf
	v_add_f32_dpp v57, v57, v57 quad_perm:[2,3,0,1] row_mask:0xf bank_mask:0xf
	v_sub_f32_e32 v60, v56, v55
	v_mul_f32_e32 v58, v57, v57
	v_cmp_gt_f32_e32 vcc, 0, v60
	v_mul_f32_e32 v59, v60, v60
	v_fmac_f32_e32 v59, 4.0, v58
	v_sqrt_f32_e32 v59, v59
	v_mul_f32_e32 v63, v62, v41
	v_mul_f32_e32 v43, v62, v40
	v_fma_f32 v40, v61, v40, -v63
	v_fma_f32 v41, v61, v41, v43
	v_add_f32_e64 v59, |v60|, v59
	v_add_f32_e32 v59, 0x0da24260, v59
	v_rcp_f32_e32 v59, v59
	v_add_f32_e32 v58, v57, v57
	v_mul_f32_e32 v59, v58, v59
	v_cndmask_b32_e64 v59, v59, -v59, vcc
	v_fma_f32 v58, v59, v59, 1.0
	v_rsq_f32_e32 v61, v58
	s_nop 0
	v_mul_f32_e32 v62, v61, v59
	v_mul_f32_e32 v55, v62, v54
	v_mul_f32_e32 v56, v62, v52
	v_fma_f32 v52, v61, v52, -v55
	v_fma_f32 v54, v61, v54, v56
	v_mul_f32_e32 v55, v53, v53
	v_mul_f32_e32 v56, v54, v54
	v_mul_f32_e32 v57, v53, v54
	v_add_f32_dpp v55, v55, v55 quad_perm:[1,0,3,2] row_mask:0xf bank_mask:0xf
	v_add_f32_dpp v56, v56, v56 quad_perm:[1,0,3,2] row_mask:0xf bank_mask:0xf
	v_add_f32_dpp v57, v57, v57 quad_perm:[1,0,3,2] row_mask:0xf bank_mask:0xf
	v_add_f32_dpp v55, v55, v55 quad_perm:[2,3,0,1] row_mask:0xf bank_mask:0xf
	v_add_f32_dpp v56, v56, v56 quad_perm:[2,3,0,1] row_mask:0xf bank_mask:0xf
	v_add_f32_dpp v57, v57, v57 quad_perm:[2,3,0,1] row_mask:0xf bank_mask:0xf
	v_sub_f32_e32 v60, v56, v55
	v_mul_f32_e32 v58, v57, v57
	v_cmp_gt_f32_e32 vcc, 0, v60
	v_mul_f32_e32 v59, v60, v60
	v_fmac_f32_e32 v59, 4.0, v58
	v_sqrt_f32_e32 v59, v59
	v_mul_f32_e32 v63, v62, v42
	v_mul_f32_e32 v43, v62, v40
	v_fma_f32 v40, v61, v40, -v63
	v_fma_f32 v42, v61, v42, v43
	v_add_f32_e64 v59, |v60|, v59
	v_add_f32_e32 v59, 0x0da24260, v59
	v_rcp_f32_e32 v59, v59
	v_add_f32_e32 v58, v57, v57
	v_mul_f32_e32 v59, v58, v59
	v_cndmask_b32_e64 v59, v59, -v59, vcc
	v_fma_f32 v58, v59, v59, 1.0
	v_rsq_f32_e32 v61, v58
	s_nop 0
	v_mul_f32_e32 v62, v61, v59
	v_mul_f32_e32 v55, v62, v54
	v_mul_f32_e32 v56, v62, v53
	v_fma_f32 v53, v61, v53, -v55
	v_fma_f32 v54, v61, v54, v56
	v_mul_f32_e32 v55, v52, v52
	v_mul_f32_e32 v56, v53, v53
	v_mul_f32_e32 v57, v52, v53
	v_add_f32_dpp v55, v55, v55 quad_perm:[1,0,3,2] row_mask:0xf bank_mask:0xf
	v_add_f32_dpp v56, v56, v56 quad_perm:[1,0,3,2] row_mask:0xf bank_mask:0xf
	v_add_f32_dpp v57, v57, v57 quad_perm:[1,0,3,2] row_mask:0xf bank_mask:0xf
	v_add_f32_dpp v55, v55, v55 quad_perm:[2,3,0,1] row_mask:0xf bank_mask:0xf
	v_add_f32_dpp v56, v56, v56 quad_perm:[2,3,0,1] row_mask:0xf bank_mask:0xf
	v_add_f32_dpp v57, v57, v57 quad_perm:[2,3,0,1] row_mask:0xf bank_mask:0xf
	v_sub_f32_e32 v60, v56, v55
	v_mul_f32_e32 v58, v57, v57
	v_cmp_gt_f32_e32 vcc, 0, v60
	v_mul_f32_e32 v59, v60, v60
	v_fmac_f32_e32 v59, 4.0, v58
	v_sqrt_f32_e32 v59, v59
	v_mul_f32_e32 v63, v62, v42
	v_mul_f32_e32 v43, v62, v41
	v_fma_f32 v41, v61, v41, -v63
	v_fma_f32 v42, v61, v42, v43
	v_add_f32_e64 v59, |v60|, v59
	v_add_f32_e32 v59, 0x0da24260, v59
	v_rcp_f32_e32 v59, v59
	v_add_f32_e32 v58, v57, v57
	v_mul_f32_e32 v59, v58, v59
	v_cndmask_b32_e64 v59, v59, -v59, vcc
	v_fma_f32 v58, v59, v59, 1.0
	v_rsq_f32_e32 v61, v58
	s_nop 0
	v_mul_f32_e32 v62, v61, v59
	v_mul_f32_e32 v55, v62, v53
	v_mul_f32_e32 v56, v62, v52
	v_fma_f32 v52, v61, v52, -v55
	v_fma_f32 v53, v61, v53, v56
	v_mul_f32_e32 v55, v52, v52
	v_mul_f32_e32 v56, v54, v54
	v_mul_f32_e32 v57, v52, v54
	v_add_f32_dpp v55, v55, v55 quad_perm:[1,0,3,2] row_mask:0xf bank_mask:0xf
	v_add_f32_dpp v56, v56, v56 quad_perm:[1,0,3,2] row_mask:0xf bank_mask:0xf
	v_add_f32_dpp v57, v57, v57 quad_perm:[1,0,3,2] row_mask:0xf bank_mask:0xf
	v_add_f32_dpp v55, v55, v55 quad_perm:[2,3,0,1] row_mask:0xf bank_mask:0xf
	v_add_f32_dpp v56, v56, v56 quad_perm:[2,3,0,1] row_mask:0xf bank_mask:0xf
	v_add_f32_dpp v57, v57, v57 quad_perm:[2,3,0,1] row_mask:0xf bank_mask:0xf
	v_sub_f32_e32 v60, v56, v55
	v_mul_f32_e32 v58, v57, v57
	v_cmp_gt_f32_e32 vcc, 0, v60
	v_mul_f32_e32 v59, v60, v60
	v_fmac_f32_e32 v59, 4.0, v58
	v_sqrt_f32_e32 v59, v59
	v_mul_f32_e32 v63, v62, v41
	v_mul_f32_e32 v43, v62, v40
	v_fma_f32 v40, v61, v40, -v63
	v_fma_f32 v41, v61, v41, v43
	v_add_f32_e64 v59, |v60|, v59
	v_add_f32_e32 v59, 0x0da24260, v59
	v_rcp_f32_e32 v59, v59
	v_add_f32_e32 v58, v57, v57
	v_mul_f32_e32 v59, v58, v59
	v_cndmask_b32_e64 v59, v59, -v59, vcc
	v_fma_f32 v58, v59, v59, 1.0
	v_rsq_f32_e32 v61, v58
	s_nop 0
	v_mul_f32_e32 v62, v61, v59
	v_mul_f32_e32 v55, v62, v54
	v_mul_f32_e32 v56, v62, v52
	v_fma_f32 v52, v61, v52, -v55
	v_fma_f32 v54, v61, v54, v56
	v_mul_f32_e32 v55, v53, v53
	v_mul_f32_e32 v56, v54, v54
	v_mul_f32_e32 v57, v53, v54
	v_add_f32_dpp v55, v55, v55 quad_perm:[1,0,3,2] row_mask:0xf bank_mask:0xf
	v_add_f32_dpp v56, v56, v56 quad_perm:[1,0,3,2] row_mask:0xf bank_mask:0xf
	v_add_f32_dpp v57, v57, v57 quad_perm:[1,0,3,2] row_mask:0xf bank_mask:0xf
	v_add_f32_dpp v55, v55, v55 quad_perm:[2,3,0,1] row_mask:0xf bank_mask:0xf
	v_add_f32_dpp v56, v56, v56 quad_perm:[2,3,0,1] row_mask:0xf bank_mask:0xf
	v_add_f32_dpp v57, v57, v57 quad_perm:[2,3,0,1] row_mask:0xf bank_mask:0xf
	v_sub_f32_e32 v60, v56, v55
	v_mul_f32_e32 v58, v57, v57
	v_cmp_gt_f32_e32 vcc, 0, v60
	v_mul_f32_e32 v59, v60, v60
	v_fmac_f32_e32 v59, 4.0, v58
	v_sqrt_f32_e32 v59, v59
	v_mul_f32_e32 v63, v62, v42
	v_mul_f32_e32 v43, v62, v40
	v_fma_f32 v40, v61, v40, -v63
	v_fma_f32 v42, v61, v42, v43
	v_add_f32_e64 v59, |v60|, v59
	v_add_f32_e32 v59, 0x0da24260, v59
	v_rcp_f32_e32 v59, v59
	v_add_f32_e32 v58, v57, v57
	v_mul_f32_e32 v59, v58, v59
	v_cndmask_b32_e64 v59, v59, -v59, vcc
	v_fma_f32 v58, v59, v59, 1.0
	v_rsq_f32_e32 v61, v58
	s_nop 0
	v_mul_f32_e32 v62, v61, v59
	v_mul_f32_e32 v55, v62, v54
	v_mul_f32_e32 v56, v62, v53
	v_fma_f32 v53, v61, v53, -v55
	v_fma_f32 v54, v61, v54, v56
	v_mul_f32_e32 v63, v62, v42
	v_mul_f32_e32 v43, v62, v41
	v_fma_f32 v41, v61, v41, -v63
	v_fma_f32 v42, v61, v42, v43
	v_mul_f32_e32 v55, v52, v52
	v_mul_f32_e32 v56, v53, v53
	v_mul_f32_e32 v57, v54, v54
	v_add_f32_dpp v55, v55, v55 quad_perm:[1,0,3,2] row_mask:0xf bank_mask:0xf
	v_add_f32_dpp v56, v56, v56 quad_perm:[1,0,3,2] row_mask:0xf bank_mask:0xf
	v_add_f32_dpp v57, v57, v57 quad_perm:[1,0,3,2] row_mask:0xf bank_mask:0xf
	v_add_f32_dpp v55, v55, v55 quad_perm:[2,3,0,1] row_mask:0xf bank_mask:0xf
	v_add_f32_dpp v56, v56, v56 quad_perm:[2,3,0,1] row_mask:0xf bank_mask:0xf
	v_add_f32_dpp v57, v57, v57 quad_perm:[2,3,0,1] row_mask:0xf bank_mask:0xf
	v_cmp_le_f32_e64 s[28:29], v55, v56
	v_cmp_le_f32_e64 s[30:31], v55, v57
	v_cmp_lt_f32_e32 vcc, v57, v56
	s_and_b64 s[28:29], s[28:29], s[30:31]
	s_andn2_b64 s[30:31], vcc, s[28:29]
	v_cndmask_b32_e64 v44, v52, v53, s[28:29]
	v_cndmask_b32_e64 v45, v54, v53, s[30:31]
	v_cndmask_b32_e64 v46, v40, v41, s[28:29]
	v_cndmask_b32_e64 v47, v42, v41, s[30:31]
	v_mul_f32_e32 v58, v44, v44
	s_nop 1
	v_add_f32_dpp v58, v58, v58 quad_perm:[1,0,3,2] row_mask:0xf bank_mask:0xf
	s_nop 1
	v_add_f32_dpp v58, v58, v58 quad_perm:[2,3,0,1] row_mask:0xf bank_mask:0xf
	v_max_f32_e32 v58, 0x3aa2425, v58
	v_rsq_f32_e32 v58, v58
	s_nop 0
	v_mul_f32_e32 v48, v44, v58
	v_mul_f32_e32 v59, v48, v45
	s_nop 1
	v_add_f32_dpp v59, v59, v59 quad_perm:[1,0,3,2] row_mask:0xf bank_mask:0xf
	s_nop 1
	v_add_f32_dpp v59, v59, v59 quad_perm:[2,3,0,1] row_mask:0xf bank_mask:0xf
	v_fma_f32 v49, -v59, v48, v45
	v_mul_f32_e32 v58, v49, v49
	s_nop 1
	v_add_f32_dpp v58, v58, v58 quad_perm:[1,0,3,2] row_mask:0xf bank_mask:0xf
	s_nop 1
	v_add_f32_dpp v58, v58, v58 quad_perm:[2,3,0,1] row_mask:0xf bank_mask:0xf
	v_max_f32_e32 v58, 0x3aa2425, v58
	v_rsq_f32_e32 v58, v58
	s_nop 0
	v_mul_f32_e32 v50, v49, v58
	v_mov_b32_dpp v43, v47 quad_perm:[2,0,1,3] row_mask:0xf bank_mask:0xf
	v_mov_b32_dpp v63, v47 quad_perm:[1,2,0,3] row_mask:0xf bank_mask:0xf
	v_mov_b32_dpp v62, v50 quad_perm:[2,0,1,3] row_mask:0xf bank_mask:0xf
	v_mov_b32_dpp v61, v50 quad_perm:[1,2,0,3] row_mask:0xf bank_mask:0xf
	v_mul_f32_dpp v60, v46, v43 quad_perm:[1,2,0,3] row_mask:0xf bank_mask:0xf
	v_mul_f32_dpp v51, v48, v62 quad_perm:[1,2,0,3] row_mask:0xf bank_mask:0xf
	s_nop 0
	v_fmac_f32_dpp v60, -v46, v63 quad_perm:[2,0,1,3] row_mask:0xf bank_mask:0xf
	v_fmac_f32_dpp v51, -v48, v61 quad_perm:[2,0,1,3] row_mask:0xf bank_mask:0xf
	v_mul_f32_dpp v52, v46, v48 quad_perm:[0,0,0,0] row_mask:0xf bank_mask:0xf
	v_mul_f32_dpp v53, v46, v48 quad_perm:[1,1,1,1] row_mask:0xf bank_mask:0xf
	v_mul_f32_dpp v54, v46, v48 quad_perm:[2,2,2,2] row_mask:0xf bank_mask:0xf
	v_fmac_f32_dpp v52, v47, v50 quad_perm:[0,0,0,0] row_mask:0xf bank_mask:0xf
	v_fmac_f32_dpp v53, v47, v50 quad_perm:[1,1,1,1] row_mask:0xf bank_mask:0xf
	v_fmac_f32_dpp v54, v47, v50 quad_perm:[2,2,2,2] row_mask:0xf bank_mask:0xf
	v_fmac_f32_dpp v52, v60, v51 quad_perm:[0,0,0,0] row_mask:0xf bank_mask:0xf
	v_fmac_f32_dpp v53, v60, v51 quad_perm:[1,1,1,1] row_mask:0xf bank_mask:0xf
	v_fmac_f32_dpp v54, v60, v51 quad_perm:[2,2,2,2] row_mask:0xf bank_mask:0xf
	v_mov_b32_e32 v55, 0
	v_writelane_b32 v55, s32, 48
	v_writelane_b32 v55, s33, 49
	v_writelane_b32 v55, s34, 50
	v_mul_f32_e32 v55, 0xbc800000, v55
	v_mul_f32_e32 v56, v55, v52
	v_mul_f32_e32 v57, v55, v53
	v_mul_f32_e32 v58, v55, v54
	v_add_f32_dpp v56, v56, v56 quad_perm:[1,0,3,2] row_mask:0xf bank_mask:0xf
	v_add_f32_dpp v57, v57, v57 quad_perm:[1,0,3,2] row_mask:0xf bank_mask:0xf
	v_add_f32_dpp v58, v58, v58 quad_perm:[1,0,3,2] row_mask:0xf bank_mask:0xf
	v_add_f32_dpp v56, v56, v56 quad_perm:[2,3,0,1] row_mask:0xf bank_mask:0xf
	v_add_f32_dpp v57, v57, v57 quad_perm:[2,3,0,1] row_mask:0xf bank_mask:0xf
	v_add_f32_dpp v58, v58, v58 quad_perm:[2,3,0,1] row_mask:0xf bank_mask:0xf
	v_cndmask_b32_e64 v52, v52, v56, s[26:27]
	v_cndmask_b32_e64 v53, v53, v57, s[26:27]
	v_cndmask_b32_e64 v54, v54, v58, s[26:27]
	v_subrev_u32_e32 v59, 48, v0
	v_lshlrev_b32_e32 v59, 4, v59
	s_mov_b32 s20, 0
	s_mov_b32 s21, 0xf0000
	s_mov_b64 exec, s[20:21]
	ds_write_b96 v59, v[52:54] offset:24576
	s_mov_b64 exec, -1
	s_waitcnt lgkmcnt(0)
	s_branch .Ljoin
.Lbulk_waves:
	s_mov_b32 m0, s18
	s_nop 0
	global_load_lds_dwordx4 v1, s[40:41] sc1 nt
	global_load_lds_dwordx4 v1, s[40:41] offset:1024 sc1 nt
	global_load_lds_dwordx4 v1, s[40:41] offset:2048 sc1 nt
	global_load_lds_dwordx4 v1, s[40:41] offset:3072 sc1 nt
	s_add_u32 m0, s18, 0x1000
	s_nop 0
	global_load_lds_dwordx4 v1, s[42:43] sc1 nt
	s_and_saveexec_b64 s[16:17], s[14:15]
	global_load_lds_dwordx4 v1, s[42:43] offset:1024 sc1 nt
	s_mov_b64 exec, s[16:17]
	s_waitcnt vmcnt(0)
	s_waitcnt lgkmcnt(0)
	s_barrier
